# GQA units: the four HBM weight loads of the rider are issued after the step's K/V tile loads, counted waits re-derived, so the K/V waits no longer wait for HBM
# speedup vs baseline: 1.0097x; 1.0097x over previous
; DI void attn_unit_a8(unsigned char* lds, const AttnArgs& a) {
;     ...
;     auto w_cvt = [&]() __attribute__((always_inline)) { unsigned char* t8 = lds + AT_WT + wn4 * WPITCH + 4 * wid;
; #pragma unroll
;         for (int j = 0; j < 4; ++j) *(unsigned*)(t8 + j * WPITCH) = pk4_fp8_mul64(wq[0][j], wq[1][j], wq[2][j], wq[3][j]); };
;     const int wcol = tid >> 1, whalf = tid & 1;
;     const unsigned wper_gu = (unsigned)((wcol >> 7) * 256 + (wcol & 96) + invperm32(wcol & 31)) * 1024u + 16u * whalf;
;     const unsigned wper_dn = (unsigned)fwd_lane16(wcol) * 1024u + 16u * whalf;
;     auto w_store = [&](int j) __attribute__((always_inline)) { const float* src; unsigned char* dst; int ld, n0, k0; bool gu; w_decode(j, src, dst, ld, n0, k0, gu);
;         const int nb = n0 >> 8; const unsigned uni = (unsigned)(gu ? (nb & 3) * 512 + (nb >> 2) * 128 : nb * 256) * 1024u + (unsigned)k0;
;         const unsigned off = (gu ? wper_gu : wper_dn) + uni;
;         const unsigned* t = (const unsigned*)(lds + AT_WT + wcol * WPITCH + 16 * whalf);
;         *(u32x4*)(dst + off) = (u32x4){t[0], t[1], t[2], t[3]}; };
;     const bool wrider = a.wl >= 0;
;     if (wrider) w_issue(0);
;     gload(a.t0, kregA, vregA); gload(a.t0 + 1 < a.t1 ? a.t0 + 1 : a.t0, kregB, vregB);
;     lstore(0, kregA, vregA); lstore(1, kregB, vregB);
;     __syncthreads();
;     asm volatile("" : "+v"(qf8));
;     if (a.t0 + 2 < a.t1) gload(a.t0 + 2, kregA, vregA);
;     f32x16 sx0, sx1, sy0, sy1;
;     sx0 = mfma8(kread(lds, 0), qf8, cinit); sx1 = mfma8(kread(lds, 1), qf8, cinit);
;     int slot = 0;
;     auto step = [&](int t, u32x2& kl, u32x2& vl, const u32x2& ks, const u32x2& vs, f32x16& c0, f32x16& c1, f32x16& n0, f32x16& n1, const int hk, const int wj) __attribute__((always_inline)) {
;         const int slot1 = slot == 2 ? 0 : slot + 1, slot2 = slot1 == 2 ? 0 : slot1 + 1;
;         if (hk == 1) { w_cvt(); w_issue(wj + 1 < AT_NWT ? wj + 1 : AT_NWT - 1); }
;         if (hk == 2) w_store(wj);
;         { const int tn = t + 3; gload(tn < a.t1 ? tn : a.t1 - 1, kl, vl); }
;         const unsigned char* Kb = lds + slot * AT_BUFB; const unsigned char* Kn = lds + slot1 * AT_BUFB;
;         const v8i k0 = kread(Kn, 0), k1 = kread(Kn, 1), v0 = vread(Kb, 0), v1 = vread(Kb, 1);
;         n0 = mfma8(k0, qf8, cinit); n1 = mfma8(k1, qf8, cinit);
;         expsum(c0); expsum(c1);
;         const v8i P = pack8(c0, c1);
.LBB0_702:
	s_lshl_b32 s4, s14, 1
	s_waitcnt lgkmcnt(0)
	s_lshr_b32 s12, s14, 3
	s_and_b32 s4, s4, 0x600
	s_and_b32 s12, s12, 0x80
	s_or_b32 s4, s4, s12
	s_and_b64 s[10:11], s[10:11], exec
	s_cselect_b32 s4, s4, s14
	s_and_b32 s10, s24, 3
	s_add_i32 s10, s63, s10
	s_lshl_b32 s10, s10, 5
	s_lshl_b32 s4, s4, 10
	s_add_i32 s15, s4, s10
	s_min_i32 s4, s56, 63
	s_cmp_lt_u32 s56, 60
	s_cselect_b64 s[10:11], -1, 0
	s_lshl_b32 s4, s4, 6
	v_pk_add_f32 v[48:49], v[146:147], v[110:111]
	s_add_i32 s14, s4, 0x100
	s_add_i32 s63, s4, 0xfffff100
	v_pk_add_f32 v[46:47], v[150:151], v[108:109]
	v_pk_add_f32 v[48:49], v[148:149], v[48:49]
	s_and_b64 s[12:13], s[10:11], exec
	v_pk_add_f32 v[46:47], v[142:143], v[46:47]
	v_pk_add_f32 v[48:49], v[58:59], v[48:49]
	s_cselect_b32 s12, s14, s63
	s_add_i32 s25, s25, 1
	v_pk_add_f32 v[46:47], v[144:145], v[46:47]
	v_pk_add_f32 v[48:49], v[60:61], v[48:49]
	s_and_b64 s[6:7], s[6:7], exec
	v_pk_add_f32 v[46:47], v[52:53], v[46:47]
	v_pk_add_f32 v[48:49], v[50:51], v[48:49]
	s_cselect_b32 s14, 0, s25
	v_pk_add_f32 v[46:47], v[56:57], v[46:47]
	v_pk_add_f32 v[48:49], v[54:55], v[48:49]
	s_mul_i32 s6, s14, 0x4680
	v_pk_add_f32 v[38:39], v[38:39], v[46:47]
	v_pk_add_f32 v[36:37], v[36:37], v[48:49]
	v_add_u32_e32 v48, 0xd808, v163
	v_add_u32_e32 v134, s6, v157
	v_pk_add_f32 v[50:51], v[42:43], v[38:39]
	v_pk_add_f32 v[108:109], v[40:41], v[36:37]
	v_add_u32_e32 v45, 0xd800, v163
	ds_read_b128 v[36:39], v134
	ds_read_b128 v[40:43], v134 offset:16
	ds_read2_b32 v[46:47], v45 offset1:1
	ds_read2_b32 v[48:49], v48 offset1:1
	v_pk_add_f32 v[110:111], v[34:35], v[50:51]
	v_add_u32_e32 v34, v44, v158
	v_lshl_or_b32 v34, v34, 10, v160
	v_add_u32_e32 v34, s15, v34
	s_waitcnt lgkmcnt(0)
	global_store_dwordx4 v34, v[46:49], s[8:9]
	v_add_u32_e32 v34, s12, v154
	s_and_b64 s[8:9], s[10:11], exec
	v_ashrrev_i32_e32 v35, 31, v34
	s_cselect_b32 s9, s59, s61
	s_cselect_b32 s8, s58, s60
	v_lshlrev_b64 v[34:35], 7, v[34:35]
	v_mfma_f32_32x32x64_f8f6f4 v[50:65], v[36:43], v[98:105], 0
	v_lshl_add_u64 v[42:43], s[8:9], 0, v[34:35]
	v_lshl_add_u64 v[42:43], v[42:43], 0, v[130:131]
	ds_read_b128 v[34:37], v134 offset:2560
	ds_read_b128 v[38:41], v134 offset:2576
	global_load_dwordx2 v[134:135], v[42:43], off
	v_lshl_add_u64 v[42:43], v[132:133], 0, s[4:5]
	global_load_dwordx2 v[136:137], v[42:43], off offset:256
	v_exp_f32_e32 v82, v82
	v_exp_f32_e32 v83, v83
	v_exp_f32_e32 v86, v86
	v_exp_f32_e32 v87, v87
	v_exp_f32_e32 v90, v90
	v_exp_f32_e32 v91, v91
	v_exp_f32_e32 v94, v94
	v_exp_f32_e32 v95, v95
	v_exp_f32_e32 v150, v66
	v_exp_f32_e32 v151, v67
	v_exp_f32_e32 v174, v70
	v_exp_f32_e32 v175, v71
	v_exp_f32_e32 v74, v74
	v_exp_f32_e32 v75, v75
	v_exp_f32_e32 v78, v78
	v_exp_f32_e32 v79, v79
	ds_read_b128 v[142:145], v164 offset:5120
	ds_read_b128 v[146:149], v164 offset:5136
	ds_read_b128 v[166:169], v164 offset:7680
	ds_read_b128 v[170:173], v164 offset:7696
	v_exp_f32_e32 v84, v84
	v_exp_f32_e32 v85, v85
	v_exp_f32_e32 v88, v88
	v_exp_f32_e32 v89, v89
	v_exp_f32_e32 v92, v92
	v_exp_f32_e32 v93, v93
	v_exp_f32_e32 v96, v96
	v_exp_f32_e32 v97, v97
	v_exp_f32_e32 v164, v68
	v_exp_f32_e32 v165, v69
	v_exp_f32_e32 v176, v72
	v_exp_f32_e32 v177, v73
	v_exp_f32_e32 v76, v76
	v_exp_f32_e32 v77, v77
	v_exp_f32_e32 v80, v80
	v_exp_f32_e32 v81, v81
	s_nop 0
	s_nop 0
	s_nop 0
	s_nop 0
	s_nop 0
	s_nop 0
	s_nop 0
	s_nop 0
	v_cvt_scalef32_pk_fp8_f32 v66, v82, v83, s48
	v_cvt_scalef32_pk_fp8_f32 v70, v150, v151, s48
	v_cvt_scalef32_pk_fp8_f32 v67, v86, v87, s48
	v_cvt_scalef32_pk_fp8_f32 v71, v174, v175, s48
	v_cvt_scalef32_pk_fp8_f32 v68, v90, v91, s48
	v_cvt_scalef32_pk_fp8_f32 v72, v74, v75, s48
	v_cvt_scalef32_pk_fp8_f32 v69, v94, v95, s48
	v_cvt_scalef32_pk_fp8_f32 v73, v78, v79, s48
	v_cvt_scalef32_pk_fp8_f32 v66, v84, v85, s48 op_sel:[0,0,0,1]
	v_cvt_scalef32_pk_fp8_f32 v70, v164, v165, s48 op_sel:[0,0,0,1]
	v_cvt_scalef32_pk_fp8_f32 v67, v88, v89, s48 op_sel:[0,0,0,1]
	v_cvt_scalef32_pk_fp8_f32 v71, v176, v177, s48 op_sel:[0,0,0,1]
	v_cvt_scalef32_pk_fp8_f32 v68, v92, v93, s48 op_sel:[0,0,0,1]
	v_cvt_scalef32_pk_fp8_f32 v72, v76, v77, s48 op_sel:[0,0,0,1]
	v_cvt_scalef32_pk_fp8_f32 v69, v96, v97, s48 op_sel:[0,0,0,1]
	v_cvt_scalef32_pk_fp8_f32 v73, v80, v81, s48 op_sel:[0,0,0,1]
	s_waitcnt lgkmcnt(4)
	v_mfma_f32_32x32x64_f8f6f4 v[34:49], v[34:41], v[98:105], 0
	v_add_f32_e64 v110, v110, v82
	v_add_f32_e64 v111, v111, v83
	v_add_f32_e64 v82, v108, v84
	v_add_f32_e64 v83, v109, v85
	v_add_f32_e64 v84, v86, v110
	v_add_f32_e64 v85, v87, v111
	v_add_f32_e64 v82, v88, v82
	v_add_f32_e64 v83, v89, v83
	s_addk_i32 s6, 0x4680
	v_add_f32_e64 v84, v90, v84
	v_add_f32_e64 v85, v91, v85
	v_add_f32_e64 v82, v92, v82
	v_add_f32_e64 v83, v93, v83
	s_cmp_lg_u32 s14, 2
	v_pk_add_f32 v[82:83], v[96:97], v[82:83]
	v_pk_add_f32 v[84:85], v[94:95], v[84:85]
	s_cselect_b32 s4, s6, 0
	v_pk_add_f32 v[84:85], v[150:151], v[84:85]
	v_pk_add_f32 v[82:83], v[164:165], v[82:83]
	s_add_i32 s4, s4, 0
	v_pk_add_f32 v[82:83], v[176:177], v[82:83]
	s_waitcnt lgkmcnt(2)
	v_mfma_f32_32x32x64_f8f6f4 v[18:33], v[142:149], v[66:73], v[18:33]
	v_add_f32_e64 v84, v174, v84
	v_add_f32_e64 v85, v175, v85
	v_add_f32_e64 v76, v76, v82
	v_add_f32_e64 v77, v77, v83
	v_add_f32_e64 v74, v74, v84
	v_add_f32_e64 v75, v75, v85
	s_add_i32 s24, s24, 1
	s_add_i32 s56, s56, 2
	s_addk_i32 s19, 0x80
	v_add_f32_e64 v110, v80, v76
	v_add_f32_e64 v111, v81, v77
	v_add_f32_e64 v108, v78, v74
	v_add_f32_e64 v109, v79, v75
	s_cmp_lg_u32 s24, 24
	s_waitcnt lgkmcnt(0)
	v_mfma_f32_32x32x64_f8f6f4 v[2:17], v[166:173], v[66:73], v[2:17]
	v_add_u32_e32 v66, s4, v155
	s_waitcnt vmcnt(8)
	ds_write_b64 v66, v[138:139]
	v_add_u32_e32 v66, s4, v156
	v_add_u32_e32 v66, 0x1400, v66
	s_waitcnt vmcnt(7)
	ds_write2_b32 v66, v140, v141 offset1:8
	s_waitcnt lgkmcnt(0)
	s_barrier
	s_cbranch_scc0 .LBB0_712
.LBB0_703:
	s_min_u32 s15, s24, 22
	s_add_i32 s15, s15, 1
	s_lshl_b32 s4, s15, 7
	s_and_b32 s4, s4, 0x1e00
	s_nop 0
	s_nop 0
	s_add_i32 s6, s4, s62
	s_waitcnt vmcnt(3)
	v_cvt_scalef32_pk_fp8_f32 v66, v116, v112, s47
	v_cvt_scalef32_pk_fp8_f32 v67, v117, v113, s47
	s_mul_hi_u32 s4, s6, 0xaaaaaaab
	v_cvt_scalef32_pk_fp8_f32 v66, v120, v124, s47 op_sel:[0,0,0,1]
	v_cvt_scalef32_pk_fp8_f32 v67, v121, v125, s47 op_sel:[0,0,0,1]
	v_add_u32_e32 v68, 0xd800, v162
	s_lshr_b32 s4, s4, 6
	ds_write2_b32 v68, v66, v67 offset1:9
	s_nop 0
	s_nop 0
	s_mul_i32 s63, s4, 0xffffffa0
	v_cvt_scalef32_pk_fp8_f32 v66, v118, v114, s47
	v_cvt_scalef32_pk_fp8_f32 v67, v119, v115, s47
	s_add_i32 s63, s63, s6
	v_cvt_scalef32_pk_fp8_f32 v66, v122, v126, s47 op_sel:[0,0,0,1]
	v_cvt_scalef32_pk_fp8_f32 v67, v123, v127, s47 op_sel:[0,0,0,1]
	s_mov_b64 s[10:11], s[0:1]
	s_cmp_gt_i32 s63, 63
	s_mov_b64 s[12:13], -1
	ds_write2_b32 v68, v66, v67 offset0:18 offset1:27
	s_cbranch_scc0 .LBB0_705
	s_load_dwordx2 s[6:7], s[10:11], 0xc0
	s_lshl_b64 s[8:9], s[4:5], 22
	s_mov_b64 s[12:13], 0
	s_waitcnt lgkmcnt(0)
	s_add_u32 s6, s6, s8
	s_addc_u32 s7, s7, s9
	s_and_b32 s8, s63, 0x7ffffffc
	s_sub_i32 s25, s8, 64

; DI void attn_unit_a8(unsigned char* lds, const AttnArgs& a) {
;     ...
;     auto w_issue = [&](int j) __attribute__((always_inline)) { const float* src; unsigned char* dst; int ld, n0, k0; bool gu; w_decode(j, src, dst, ld, n0, k0, gu);
;         const float* p = src + (size_t)(k0 + 4 * wid) * ld + n0 + wn4;
;         wq[0] = __builtin_nontemporal_load((const f32x4*)p); wq[1] = __builtin_nontemporal_load((const f32x4*)(p + ld));
;         wq[2] = __builtin_nontemporal_load((const f32x4*)(p + (size_t)2 * ld)); wq[3] = __builtin_nontemporal_load((const f32x4*)(p + (size_t)3 * ld)); };
;     auto w_cvt = [&]() __attribute__((always_inline)) { unsigned char* t8 = lds + AT_WT + wn4 * WPITCH + 4 * wid;
; #pragma unroll
;         for (int j = 0; j < 4; ++j) *(unsigned*)(t8 + j * WPITCH) = pk4_fp8_mul64(wq[0][j], wq[1][j], wq[2][j], wq[3][j]); };
;     const int wcol = tid >> 1, whalf = tid & 1;
;     const unsigned wper_gu = (unsigned)((wcol >> 7) * 256 + (wcol & 96) + invperm32(wcol & 31)) * 1024u + 16u * whalf;
;     const unsigned wper_dn = (unsigned)fwd_lane16(wcol) * 1024u + 16u * whalf;
;     auto w_store = [&](int j) __attribute__((always_inline)) { const float* src; unsigned char* dst; int ld, n0, k0; bool gu; w_decode(j, src, dst, ld, n0, k0, gu);
;         const int nb = n0 >> 8; const unsigned uni = (unsigned)(gu ? (nb & 3) * 512 + (nb >> 2) * 128 : nb * 256) * 1024u + (unsigned)k0;
;         const unsigned off = (gu ? wper_gu : wper_dn) + uni;
;         const unsigned* t = (const unsigned*)(lds + AT_WT + wcol * WPITCH + 16 * whalf);
;         *(u32x4*)(dst + off) = (u32x4){t[0], t[1], t[2], t[3]}; };
;     const bool wrider = a.wl >= 0;
;     if (wrider) w_issue(0);
;     gload(a.t0, kregA, vregA); gload(a.t0 + 1 < a.t1 ? a.t0 + 1 : a.t0, kregB, vregB);
;     lstore(0, kregA, vregA); lstore(1, kregB, vregB);
;     __syncthreads();
;     asm volatile("" : "+v"(qf8));
;     if (a.t0 + 2 < a.t1) gload(a.t0 + 2, kregA, vregA);
;     f32x16 sx0, sx1, sy0, sy1;
;     sx0 = mfma8(kread(lds, 0), qf8, cinit); sx1 = mfma8(kread(lds, 1), qf8, cinit);
;     int slot = 0;
;     auto step = [&](int t, u32x2& kl, u32x2& vl, const u32x2& ks, const u32x2& vs, f32x16& c0, f32x16& c1, f32x16& n0, f32x16& n1, const int hk, const int wj) __attribute__((always_inline)) {
;         const int slot1 = slot == 2 ? 0 : slot + 1, slot2 = slot1 == 2 ? 0 : slot1 + 1;
.LBB0_707:
	s_and_b32 s4, s15, 3
	s_add_i32 s4, s25, s4
	s_lshl_b32 s4, s4, 5
	s_add_i32 s4, s4, s16
	s_mul_hi_i32 s11, s8, s4
	s_mul_i32 s10, s8, s4
	s_lshl_b64 s[10:11], s[10:11], 2
	s_add_u32 s4, s6, s10
	s_addc_u32 s7, s7, s11
	s_lshl_b32 s6, s9, 2
	s_add_u32 s6, s4, s6
	s_addc_u32 s7, s7, 0
	v_lshl_add_u64 v[190:191], s[6:7], 0, v[106:107]
	s_lshl_b32 s4, s8, 2
	v_lshl_add_u64 v[192:193], v[190:191], 0, s[4:5]
	v_lshl_add_u64 v[194:195], v[192:193], 0, s[4:5]
	v_lshl_add_u64 v[196:197], v[194:195], 0, s[4:5]
	s_min_i32 s4, s56, 64
	s_cmp_lt_u32 s56, 61
	s_cselect_b64 s[8:9], -1, 0
	s_lshl_b32 s4, s4, 6
	s_add_i32 s12, s4, 0xc0
	s_add_i32 s13, s4, 0xfffff0c0
	s_and_b64 s[10:11], s[8:9], exec
	s_cselect_b32 s10, s12, s13
	s_add_i32 s11, s14, 1
	s_cmp_lg_u32 s14, 2
	s_cselect_b32 s25, s11, 0
	s_mul_i32 s11, s25, 0x4680
	v_add_u32_e32 v164, s11, v157
	ds_read_b128 v[66:69], v164
	ds_read_b128 v[70:73], v164 offset:16
	v_add_u32_e32 v74, s10, v154
	s_and_b64 s[6:7], s[8:9], exec
	v_ashrrev_i32_e32 v75, 31, v74
	s_cselect_b32 s6, s58, s60
	s_cselect_b32 s7, s59, s61
	v_lshlrev_b64 v[74:75], 7, v[74:75]
	v_lshl_add_u64 v[74:75], s[6:7], 0, v[74:75]
	v_lshl_add_u64 v[140:141], v[132:133], 0, s[4:5]
	s_mul_i32 s4, s14, 0x4680
	v_lshl_add_u64 v[74:75], v[74:75], 0, v[130:131]
	v_add_u32_e32 v165, s4, v157
	s_waitcnt lgkmcnt(0)
	v_mfma_f32_32x32x64_f8f6f4 v[82:97], v[66:73], v[98:105], 0
	ds_read_b128 v[66:69], v164 offset:2560
	ds_read_b128 v[70:73], v164 offset:2576
	global_load_dwordx2 v[138:139], v[74:75], off
	ds_read_b128 v[166:169], v165 offset:5120
	ds_read_b128 v[170:173], v165 offset:5136
	global_load_dwordx2 v[140:141], v[140:141], off offset:192
	global_load_dwordx4 v[116:119], v[190:191], off nt
	global_load_dwordx4 v[112:115], v[192:193], off nt
	global_load_dwordx4 v[120:123], v[194:195], off nt
	global_load_dwordx4 v[124:127], v[196:197], off nt
	v_exp_f32_e32 v150, v50
	v_exp_f32_e32 v151, v51
	v_exp_f32_e32 v146, v52
	v_exp_f32_e32 v147, v53
	v_exp_f32_e32 v142, v54
	v_exp_f32_e32 v143, v55
	v_exp_f32_e32 v148, v56
	v_exp_f32_e32 v149, v57
	v_exp_f32_e32 v144, v58
	v_exp_f32_e32 v145, v59
	v_exp_f32_e32 v52, v62
	v_exp_f32_e32 v53, v63
	v_exp_f32_e32 v56, v34
	v_exp_f32_e32 v57, v35
	v_exp_f32_e32 v38, v38
	v_exp_f32_e32 v39, v39
	v_exp_f32_e32 v42, v42
	v_exp_f32_e32 v43, v43
	v_exp_f32_e32 v34, v46
	v_exp_f32_e32 v35, v47
	v_exp_f32_e32 v58, v60
	v_exp_f32_e32 v59, v61
	v_exp_f32_e32 v60, v64
	v_exp_f32_e32 v61, v65
	v_exp_f32_e32 v50, v36
	v_exp_f32_e32 v51, v37
	v_exp_f32_e32 v54, v40
	v_exp_f32_e32 v55, v41
	v_exp_f32_e32 v36, v44
	v_exp_f32_e32 v37, v45
	v_exp_f32_e32 v40, v48
	v_exp_f32_e32 v41, v49
	s_nop 0
	s_nop 0
	s_nop 0
	s_nop 0
	s_nop 0
	s_nop 0
	s_nop 0
	s_nop 0
	v_cvt_scalef32_pk_fp8_f32 v174, v150, v151, s48
	v_cvt_scalef32_pk_fp8_f32 v178, v56, v57, s48
	v_cvt_scalef32_pk_fp8_f32 v175, v142, v143, s48
	v_cvt_scalef32_pk_fp8_f32 v179, v38, v39, s48
	v_cvt_scalef32_pk_fp8_f32 v176, v144, v145, s48
	v_cvt_scalef32_pk_fp8_f32 v180, v42, v43, s48
	v_cvt_scalef32_pk_fp8_f32 v177, v52, v53, s48
	v_cvt_scalef32_pk_fp8_f32 v181, v34, v35, s48
	v_cvt_scalef32_pk_fp8_f32 v174, v146, v147, s48 op_sel:[0,0,0,1]
	v_cvt_scalef32_pk_fp8_f32 v178, v50, v51, s48 op_sel:[0,0,0,1]
	v_cvt_scalef32_pk_fp8_f32 v175, v148, v149, s48 op_sel:[0,0,0,1]
	v_cvt_scalef32_pk_fp8_f32 v179, v54, v55, s48 op_sel:[0,0,0,1]
	v_cvt_scalef32_pk_fp8_f32 v176, v58, v59, s48 op_sel:[0,0,0,1]
	v_cvt_scalef32_pk_fp8_f32 v180, v36, v37, s48 op_sel:[0,0,0,1]
	v_cvt_scalef32_pk_fp8_f32 v177, v60, v61, s48 op_sel:[0,0,0,1]
	v_cvt_scalef32_pk_fp8_f32 v181, v40, v41, s48 op_sel:[0,0,0,1]
	s_addk_i32 s11, 0x4680
	s_cmp_eq_u32 s25, 2
	s_waitcnt lgkmcnt(0)
	v_mfma_f32_32x32x64_f8f6f4 v[18:33], v[166:173], v[174:181], v[18:33]
	ds_read_b128 v[166:169], v165 offset:7680
	ds_read_b128 v[170:173], v165 offset:7696
	s_cselect_b64 s[6:7], -1, 0
	s_and_b64 s[8:9], s[6:7], exec
	s_cselect_b32 s4, 0, s11
	s_add_i32 s4, s4, 0
	v_add_u32_e32 v44, s4, v155
	s_waitcnt vmcnt(7)
	ds_write_b64 v44, v[134:135]
	v_add_u32_e32 v44, s4, v156
	s_and_b32 s4, s19, 0xe00
	s_add_i32 s8, s4, s62
	s_mul_hi_u32 s4, s8, 0xaaaaaaab
	s_lshr_b32 s4, s4, 6
	s_mul_i32 s65, s4, 0xffffffa0
	v_add_u32_e32 v44, 0x1400, v44
	s_add_i32 s65, s65, s8
	v_mfma_f32_32x32x64_f8f6f4 v[66:81], v[66:73], v[98:105], 0
	s_mov_b64 s[8:9], s[0:1]
	s_waitcnt vmcnt(6)
	ds_write2_b32 v44, v136, v137 offset1:8
	s_waitcnt lgkmcnt(0)
	s_barrier
	s_load_dwordx2 s[12:13], s[8:9], 0xd8
	s_cmp_lt_i32 s65, 64
	s_cselect_b64 s[10:11], -1, 0
	s_cmp_gt_i32 s65, 63
	s_mov_b64 s[14:15], -1
	v_mfma_f32_32x32x64_f8f6f4 v[2:17], v[166:173], v[174:181], v[2:17]
	s_cbranch_scc0 .LBB0_709
	s_lshl_b64 s[8:9], s[4:5], 20
	s_waitcnt lgkmcnt(0)
	s_add_u32 s8, s12, s8
	s_addc_u32 s9, s13, s9
	s_add_u32 s8, s8, 0x11094000
	s_addc_u32 s9, s9, 0
	s_and_b32 s14, s65, 0x7ffffffc
	s_sub_i32 s63, s14, 64
	s_mov_b64 s[14:15], 0

; DI void attn_unit_a8(unsigned char* lds, const AttnArgs& a) {
;     ...
;     auto w_cvt = [&]() __attribute__((always_inline)) { unsigned char* t8 = lds + AT_WT + wn4 * WPITCH + 4 * wid;
; #pragma unroll
;         for (int j = 0; j < 4; ++j) *(unsigned*)(t8 + j * WPITCH) = pk4_fp8_mul64(wq[0][j], wq[1][j], wq[2][j], wq[3][j]); };
;     const int wcol = tid >> 1, whalf = tid & 1;
;     const unsigned wper_gu = (unsigned)((wcol >> 7) * 256 + (wcol & 96) + invperm32(wcol & 31)) * 1024u + 16u * whalf;
;     const unsigned wper_dn = (unsigned)fwd_lane16(wcol) * 1024u + 16u * whalf;
;     auto w_store = [&](int j) __attribute__((always_inline)) { const float* src; unsigned char* dst; int ld, n0, k0; bool gu; w_decode(j, src, dst, ld, n0, k0, gu);
;         const int nb = n0 >> 8; const unsigned uni = (unsigned)(gu ? (nb & 3) * 512 + (nb >> 2) * 128 : nb * 256) * 1024u + (unsigned)k0;
;         const unsigned off = (gu ? wper_gu : wper_dn) + uni;
;         const unsigned* t = (const unsigned*)(lds + AT_WT + wcol * WPITCH + 16 * whalf);
;         *(u32x4*)(dst + off) = (u32x4){t[0], t[1], t[2], t[3]}; };
;     const bool wrider = a.wl >= 0;
;     if (wrider) w_issue(0);
;     gload(a.t0, kregA, vregA); gload(a.t0 + 1 < a.t1 ? a.t0 + 1 : a.t0, kregB, vregB);
;     lstore(0, kregA, vregA); lstore(1, kregB, vregB);
;     __syncthreads();
;     asm volatile("" : "+v"(qf8));
;     if (a.t0 + 2 < a.t1) gload(a.t0 + 2, kregA, vregA);
;     f32x16 sx0, sx1, sy0, sy1;
;     sx0 = mfma8(kread(lds, 0), qf8, cinit); sx1 = mfma8(kread(lds, 1), qf8, cinit);
;     int slot = 0;
;     auto step = [&](int t, u32x2& kl, u32x2& vl, const u32x2& ks, const u32x2& vs, f32x16& c0, f32x16& c1, f32x16& n0, f32x16& n1, const int hk, const int wj) __attribute__((always_inline)) {
;         const int slot1 = slot == 2 ? 0 : slot + 1, slot2 = slot1 == 2 ? 0 : slot1 + 1;
;         if (hk == 1) { w_cvt(); w_issue(wj + 1 < AT_NWT ? wj + 1 : AT_NWT - 1); }
;         if (hk == 2) w_store(wj);
;         { const int tn = t + 3; gload(tn < a.t1 ? tn : a.t1 - 1, kl, vl); }
;         const unsigned char* Kb = lds + slot * AT_BUFB; const unsigned char* Kn = lds + slot1 * AT_BUFB;
;         const v8i k0 = kread(Kn, 0), k1 = kread(Kn, 1), v0 = vread(Kb, 0), v1 = vread(Kb, 1);
;         n0 = mfma8(k0, qf8, cinit); n1 = mfma8(k1, qf8, cinit);
;         expsum(c0); expsum(c1);
;         const v8i P = pack8(c0, c1);
.LBB0_1922:
	s_lshl_b32 s8, s18, 1
	s_waitcnt lgkmcnt(0)
	s_lshr_b32 s16, s18, 3
	s_and_b32 s8, s8, 0x600
	s_and_b32 s16, s16, 0x80
	s_or_b32 s8, s8, s16
	s_and_b64 s[14:15], s[14:15], exec
	v_pk_add_f32 v[54:55], v[164:165], v[108:109]
	s_cselect_b32 s8, s8, s18
	s_and_b32 s14, s50, 3
	v_pk_add_f32 v[54:55], v[154:155], v[54:55]
	s_add_i32 s14, s52, s14
	v_pk_add_f32 v[54:55], v[158:159], v[54:55]
	s_lshl_b32 s14, s14, 5
	s_lshl_b32 s8, s8, 10
	v_pk_add_f32 v[56:57], v[160:161], v[110:111]
	v_pk_add_f32 v[46:47], v[46:47], v[54:55]
	s_add_i32 s14, s8, s14
	s_add_i32 s51, s51, 1
	v_pk_add_f32 v[56:57], v[162:163], v[56:57]
	v_pk_add_f32 v[46:47], v[50:51], v[46:47]
	s_and_b64 s[12:13], s[12:13], exec
	v_pk_add_f32 v[56:57], v[152:153], v[56:57]
	v_pk_add_f32 v[40:41], v[40:41], v[46:47]
	s_cselect_b32 s18, 0, s51
	v_pk_add_f32 v[56:57], v[156:157], v[56:57]
	v_pk_add_f32 v[50:51], v[42:43], v[40:41]
	s_mul_i32 s8, s18, 0x4680
	v_pk_add_f32 v[44:45], v[44:45], v[56:57]
	v_add_u32_e32 v58, s8, v169
	v_pk_add_f32 v[110:111], v[34:35], v[50:51]
	v_add_u32_e32 v34, 0xd800, v175
	v_pk_add_f32 v[48:49], v[48:49], v[44:45]
	ds_read_b128 v[40:43], v58
	ds_read_b128 v[44:47], v58 offset:16
	v_add_u32_e32 v35, 0xd808, v175
	ds_read2_b32 v[54:55], v34 offset1:1
	ds_read2_b32 v[56:57], v35 offset1:1
	v_add_u32_e32 v50, v52, v170
	v_lshl_or_b32 v50, v50, 10, v172
	v_add_u32_e32 v50, s14, v50
	v_exp_f32_e32 v82, v82
	s_waitcnt lgkmcnt(0)
	global_store_dwordx4 v50, v[54:57], s[10:11]
	ds_read_b128 v[50:53], v58 offset:2560
	ds_read_b128 v[54:57], v58 offset:2576
	v_add_co_u32_e32 v58, vcc, s70, v148
	v_exp_f32_e32 v83, v83
	s_nop 0
	v_addc_co_u32_e32 v59, vcc, 0, v149, vcc
	global_load_dwordx2 v[136:137], v[58:59], off
	global_load_dwordx2 v[138:139], v[150:151], off offset:256
	v_exp_f32_e32 v86, v86
	v_exp_f32_e32 v87, v87
	v_exp_f32_e32 v90, v90
	v_exp_f32_e32 v91, v91
	v_exp_f32_e32 v94, v94
	v_exp_f32_e32 v95, v95
	v_exp_f32_e32 v164, v66
	v_exp_f32_e32 v165, v67
	v_exp_f32_e32 v178, v70
	v_exp_f32_e32 v179, v71
	v_exp_f32_e32 v74, v74
	v_exp_f32_e32 v75, v75
	v_exp_f32_e32 v78, v78
	v_exp_f32_e32 v79, v79
	ds_read_b128 v[148:151], v176 offset:5120
	ds_read_b128 v[152:155], v176 offset:5136
	ds_read_b128 v[156:159], v176 offset:7680
	ds_read_b128 v[160:163], v176 offset:7696
	v_exp_f32_e32 v84, v84
	v_exp_f32_e32 v85, v85
	v_exp_f32_e32 v88, v88
	v_exp_f32_e32 v89, v89
	v_exp_f32_e32 v92, v92
	v_exp_f32_e32 v93, v93
	v_exp_f32_e32 v96, v96
	v_exp_f32_e32 v97, v97
	v_exp_f32_e32 v176, v68
	v_exp_f32_e32 v177, v69
	v_exp_f32_e32 v180, v72
	v_exp_f32_e32 v181, v73
	v_exp_f32_e32 v76, v76
	v_exp_f32_e32 v77, v77
	v_exp_f32_e32 v80, v80
	v_exp_f32_e32 v81, v81
	s_nop 0
	s_nop 0
	s_nop 0
	s_nop 0
	s_nop 0
	s_nop 0
	s_nop 0
	s_nop 0
	v_cvt_scalef32_pk_fp8_f32 v66, v82, v83, s69
	v_cvt_scalef32_pk_fp8_f32 v70, v164, v165, s69
	v_cvt_scalef32_pk_fp8_f32 v67, v86, v87, s69
	v_cvt_scalef32_pk_fp8_f32 v71, v178, v179, s69
	v_cvt_scalef32_pk_fp8_f32 v68, v90, v91, s69
	v_cvt_scalef32_pk_fp8_f32 v72, v74, v75, s69
	v_cvt_scalef32_pk_fp8_f32 v69, v94, v95, s69
	v_cvt_scalef32_pk_fp8_f32 v73, v78, v79, s69
	v_pk_add_f32 v[36:37], v[36:37], v[48:49]
	v_cvt_scalef32_pk_fp8_f32 v66, v84, v85, s69 op_sel:[0,0,0,1]
	v_cvt_scalef32_pk_fp8_f32 v70, v176, v177, s69 op_sel:[0,0,0,1]
	v_cvt_scalef32_pk_fp8_f32 v67, v88, v89, s69 op_sel:[0,0,0,1]
	v_cvt_scalef32_pk_fp8_f32 v71, v180, v181, s69 op_sel:[0,0,0,1]
	v_cvt_scalef32_pk_fp8_f32 v68, v92, v93, s69 op_sel:[0,0,0,1]
	v_cvt_scalef32_pk_fp8_f32 v72, v76, v77, s69 op_sel:[0,0,0,1]
	v_cvt_scalef32_pk_fp8_f32 v69, v96, v97, s69 op_sel:[0,0,0,1]
	v_cvt_scalef32_pk_fp8_f32 v73, v80, v81, s69 op_sel:[0,0,0,1]
	v_pk_add_f32 v[108:109], v[38:39], v[36:37]
	v_mfma_f32_32x32x64_f8f6f4 v[34:49], v[40:47], v[98:105], 0
	v_add_f32_e64 v110, v110, v82
	v_add_f32_e64 v111, v111, v83
	v_add_f32_e64 v82, v108, v84
	v_add_f32_e64 v83, v109, v85
	v_add_f32_e64 v84, v86, v110
	v_add_f32_e64 v85, v87, v111
	v_add_f32_e64 v82, v88, v82
	v_add_f32_e64 v83, v89, v83
	s_addk_i32 s8, 0x4680
	v_add_f32_e64 v84, v90, v84
	v_add_f32_e64 v85, v91, v85
	v_add_f32_e64 v82, v92, v82
	v_add_f32_e64 v83, v93, v83
	s_cmp_lg_u32 s18, 2
	v_pk_add_f32 v[82:83], v[96:97], v[82:83]
	v_pk_add_f32 v[84:85], v[94:95], v[84:85]
	s_cselect_b32 s8, s8, 0
	v_pk_add_f32 v[84:85], v[164:165], v[84:85]
	v_pk_add_f32 v[82:83], v[176:177], v[82:83]
	s_add_i32 s8, s8, 0
	v_pk_add_f32 v[82:83], v[180:181], v[82:83]
	s_waitcnt lgkmcnt(4)
	v_mfma_f32_32x32x64_f8f6f4 v[50:65], v[50:57], v[98:105], 0
	v_add_f32_e64 v84, v178, v84
	v_add_f32_e64 v85, v179, v85
	v_add_f32_e64 v76, v76, v82
	v_add_f32_e64 v77, v77, v83
	v_add_f32_e64 v74, v74, v84
	v_add_f32_e64 v75, v75, v85
	s_add_i32 s50, s50, 1
	s_addk_i32 s23, 0x80
	v_add_f32_e64 v110, v80, v76
	v_add_f32_e64 v111, v81, v77
	v_add_f32_e64 v108, v78, v74
	v_add_f32_e64 v109, v79, v75
	v_lshl_add_u64 v[140:141], v[140:141], 0, s[36:37]
	s_cmp_lg_u32 s50, 24
	v_lshl_add_u64 v[142:143], v[142:143], 0, s[38:39]
	s_waitcnt lgkmcnt(2)
	v_mfma_f32_32x32x64_f8f6f4 v[18:33], v[148:155], v[66:73], v[18:33]
	s_waitcnt lgkmcnt(0)
	v_mfma_f32_32x32x64_f8f6f4 v[2:17], v[156:163], v[66:73], v[2:17]
	v_add_u32_e32 v66, s8, v131
	s_waitcnt vmcnt(8)
	ds_write_b64 v66, v[144:145]
	v_add_u32_e32 v66, s8, v168
	v_add_u32_e32 v66, 0x1400, v66
	s_waitcnt vmcnt(7)
	ds_write2_b32 v66, v146, v147 offset1:8
	s_waitcnt lgkmcnt(0)
	s_barrier
	s_cbranch_scc0 .LBB0_1931
.LBB0_1923:
	s_min_u32 s19, s50, 22
	s_add_i32 s19, s19, 1
	s_lshl_b32 s8, s19, 7
	s_and_b32 s8, s8, 0x1e00
	s_nop 0
	s_nop 0
	s_add_i32 s10, s8, s76
	s_waitcnt vmcnt(3)
	v_cvt_scalef32_pk_fp8_f32 v66, v116, v112, s66
	v_cvt_scalef32_pk_fp8_f32 v67, v117, v113, s66
	s_mul_hi_u32 s8, s10, 0xaaaaaaab
	v_cvt_scalef32_pk_fp8_f32 v66, v120, v124, s66 op_sel:[0,0,0,1]
	v_cvt_scalef32_pk_fp8_f32 v67, v121, v125, s66 op_sel:[0,0,0,1]
	v_add_u32_e32 v68, 0xd800, v174
	s_lshr_b32 s8, s8, 6
	ds_write2_b32 v68, v66, v67 offset1:9
	s_nop 0
	s_nop 0
	s_mul_i32 s52, s8, 0xffffffa0
	v_cvt_scalef32_pk_fp8_f32 v66, v118, v114, s66
	v_cvt_scalef32_pk_fp8_f32 v67, v119, v115, s66
	s_add_i32 s52, s52, s10
	v_cvt_scalef32_pk_fp8_f32 v66, v122, v126, s66 op_sel:[0,0,0,1]
	v_cvt_scalef32_pk_fp8_f32 v67, v123, v127, s66 op_sel:[0,0,0,1]
	s_mov_b64 s[14:15], s[0:1]
	s_cmp_gt_i32 s52, 63
	s_mov_b64 s[16:17], -1
	ds_write2_b32 v68, v66, v67 offset0:18 offset1:27
	s_cbranch_scc0 .LBB0_1925
	s_load_dwordx2 s[10:11], s[14:15], 0xc0
	s_lshl_b64 s[12:13], s[8:9], 22
	s_mov_b64 s[16:17], 0
	s_waitcnt lgkmcnt(0)
	s_add_u32 s10, s10, s12
	s_addc_u32 s11, s11, s13
	s_add_u32 s10, s10, 0x8000000
	s_addc_u32 s11, s11, 0
	s_and_b32 s12, s52, 0x7ffffffc
	s_sub_i32 s51, s12, 64

; DI void attn_unit_a8(unsigned char* lds, const AttnArgs& a) {
;     ...
;     auto w_issue = [&](int j) __attribute__((always_inline)) { const float* src; unsigned char* dst; int ld, n0, k0; bool gu; w_decode(j, src, dst, ld, n0, k0, gu);
;         const float* p = src + (size_t)(k0 + 4 * wid) * ld + n0 + wn4;
;         wq[0] = __builtin_nontemporal_load((const f32x4*)p); wq[1] = __builtin_nontemporal_load((const f32x4*)(p + ld));
;         wq[2] = __builtin_nontemporal_load((const f32x4*)(p + (size_t)2 * ld)); wq[3] = __builtin_nontemporal_load((const f32x4*)(p + (size_t)3 * ld)); };
;     auto w_cvt = [&]() __attribute__((always_inline)) { unsigned char* t8 = lds + AT_WT + wn4 * WPITCH + 4 * wid;
; #pragma unroll
;         for (int j = 0; j < 4; ++j) *(unsigned*)(t8 + j * WPITCH) = pk4_fp8_mul64(wq[0][j], wq[1][j], wq[2][j], wq[3][j]); };
;     const int wcol = tid >> 1, whalf = tid & 1;
;     const unsigned wper_gu = (unsigned)((wcol >> 7) * 256 + (wcol & 96) + invperm32(wcol & 31)) * 1024u + 16u * whalf;
;     const unsigned wper_dn = (unsigned)fwd_lane16(wcol) * 1024u + 16u * whalf;
;     auto w_store = [&](int j) __attribute__((always_inline)) { const float* src; unsigned char* dst; int ld, n0, k0; bool gu; w_decode(j, src, dst, ld, n0, k0, gu);
;         const int nb = n0 >> 8; const unsigned uni = (unsigned)(gu ? (nb & 3) * 512 + (nb >> 2) * 128 : nb * 256) * 1024u + (unsigned)k0;
;         const unsigned off = (gu ? wper_gu : wper_dn) + uni;
;         const unsigned* t = (const unsigned*)(lds + AT_WT + wcol * WPITCH + 16 * whalf);
;         *(u32x4*)(dst + off) = (u32x4){t[0], t[1], t[2], t[3]}; };
;     const bool wrider = a.wl >= 0;
;     if (wrider) w_issue(0);
;     gload(a.t0, kregA, vregA); gload(a.t0 + 1 < a.t1 ? a.t0 + 1 : a.t0, kregB, vregB);
;     lstore(0, kregA, vregA); lstore(1, kregB, vregB);
;     __syncthreads();
;     asm volatile("" : "+v"(qf8));
;     if (a.t0 + 2 < a.t1) gload(a.t0 + 2, kregA, vregA);
;     f32x16 sx0, sx1, sy0, sy1;
;     sx0 = mfma8(kread(lds, 0), qf8, cinit); sx1 = mfma8(kread(lds, 1), qf8, cinit);
;     int slot = 0;
;     auto step = [&](int t, u32x2& kl, u32x2& vl, const u32x2& ks, const u32x2& vs, f32x16& c0, f32x16& c1, f32x16& n0, f32x16& n1, const int hk, const int wj) __attribute__((always_inline)) {
;         const int slot1 = slot == 2 ? 0 : slot + 1, slot2 = slot1 == 2 ? 0 : slot1 + 1;
.LBB0_1927:
	s_and_b32 s8, s19, 3
	s_add_i32 s8, s51, s8
	s_lshl_b32 s8, s8, 5
	s_add_i32 s8, s8, s20
	s_mul_hi_i32 s15, s12, s8
	s_mul_i32 s14, s12, s8
	s_lshl_b64 s[14:15], s[14:15], 2
	s_add_u32 s8, s10, s14
	s_addc_u32 s11, s11, s15
	s_lshl_b32 s10, s13, 2
	s_add_u32 s10, s8, s10
	s_addc_u32 s11, s11, 0
	s_lshl_b32 s8, s12, 2
	s_add_i32 s12, s18, 1
	s_cmp_lg_u32 s18, 2
	s_cselect_b32 s51, s12, 0
	s_mul_i32 s12, s51, 0x4680
	v_add_u32_e32 v176, s12, v169
	ds_read_b128 v[66:69], v176
	ds_read_b128 v[70:73], v176 offset:16
	v_lshl_add_u64 v[190:191], s[10:11], 0, v[106:107]
	v_lshl_add_u64 v[192:193], v[190:191], 0, s[8:9]
	v_lshl_add_u64 v[148:149], v[140:141], 0, v[132:133]
	v_lshl_add_u64 v[194:195], v[192:193], 0, s[8:9]
	s_waitcnt lgkmcnt(0)
	v_mfma_f32_32x32x64_f8f6f4 v[82:97], v[66:73], v[98:105], 0
	v_add_co_u32_e32 v66, vcc, s67, v148
	v_lshl_add_u64 v[196:197], v[194:195], 0, s[8:9]
	v_addc_co_u32_e32 v67, vcc, 0, v149, vcc
	v_lshl_add_u64 v[74:75], v[142:143], 0, v[132:133]
	v_add_co_u32_e32 v150, vcc, s68, v74
	s_mul_i32 s8, s18, 0x4680
	s_nop 0
	v_addc_co_u32_e32 v151, vcc, 0, v75, vcc
	v_add_u32_e32 v177, s8, v169
	global_load_dwordx2 v[144:145], v[66:67], off
	ds_read_b128 v[66:69], v176 offset:2560
	ds_read_b128 v[70:73], v176 offset:2576
	ds_read_b128 v[178:181], v177 offset:5120
	ds_read_b128 v[182:185], v177 offset:5136
	global_load_dwordx2 v[146:147], v[150:151], off offset:192
	global_load_dwordx4 v[116:119], v[190:191], off nt
	global_load_dwordx4 v[112:115], v[192:193], off nt
	global_load_dwordx4 v[120:123], v[194:195], off nt
	global_load_dwordx4 v[124:127], v[196:197], off nt
	v_exp_f32_e32 v164, v34
	v_exp_f32_e32 v165, v35
	v_exp_f32_e32 v154, v38
	v_exp_f32_e32 v155, v39
	v_exp_f32_e32 v162, v40
	v_exp_f32_e32 v163, v41
	v_exp_f32_e32 v158, v42
	v_exp_f32_e32 v159, v43
	v_exp_f32_e32 v46, v46
	v_exp_f32_e32 v47, v47
	v_exp_f32_e32 v50, v50
	v_exp_f32_e32 v51, v51
	v_exp_f32_e32 v40, v54
	v_exp_f32_e32 v41, v55
	v_exp_f32_e32 v42, v58
	v_exp_f32_e32 v43, v59
	v_exp_f32_e32 v34, v62
	v_exp_f32_e32 v35, v63
	v_exp_f32_e32 v160, v36
	v_exp_f32_e32 v161, v37
	v_exp_f32_e32 v152, v44
	v_exp_f32_e32 v153, v45
	v_exp_f32_e32 v156, v48
	v_exp_f32_e32 v157, v49
	v_exp_f32_e32 v44, v52
	v_exp_f32_e32 v45, v53
	v_exp_f32_e32 v48, v56
	v_exp_f32_e32 v49, v57
	v_exp_f32_e32 v36, v60
	v_exp_f32_e32 v37, v61
	v_exp_f32_e32 v38, v64
	v_exp_f32_e32 v39, v65
	s_nop 0
	s_nop 0
	s_nop 0
	s_nop 0
	s_nop 0
	s_nop 0
	s_nop 0
	s_nop 0
	v_cvt_scalef32_pk_fp8_f32 v52, v164, v165, s69
	v_cvt_scalef32_pk_fp8_f32 v56, v50, v51, s69
	v_cvt_scalef32_pk_fp8_f32 v53, v154, v155, s69
	v_cvt_scalef32_pk_fp8_f32 v57, v40, v41, s69
	v_cvt_scalef32_pk_fp8_f32 v54, v158, v159, s69
	v_cvt_scalef32_pk_fp8_f32 v58, v42, v43, s69
	v_cvt_scalef32_pk_fp8_f32 v55, v46, v47, s69
	v_cvt_scalef32_pk_fp8_f32 v59, v34, v35, s69
	v_cvt_scalef32_pk_fp8_f32 v52, v160, v161, s69 op_sel:[0,0,0,1]
	v_cvt_scalef32_pk_fp8_f32 v56, v44, v45, s69 op_sel:[0,0,0,1]
	v_cvt_scalef32_pk_fp8_f32 v53, v162, v163, s69 op_sel:[0,0,0,1]
	v_cvt_scalef32_pk_fp8_f32 v57, v48, v49, s69 op_sel:[0,0,0,1]
	v_cvt_scalef32_pk_fp8_f32 v54, v152, v153, s69 op_sel:[0,0,0,1]
	v_cvt_scalef32_pk_fp8_f32 v58, v36, v37, s69 op_sel:[0,0,0,1]
	v_cvt_scalef32_pk_fp8_f32 v55, v156, v157, s69 op_sel:[0,0,0,1]
	v_cvt_scalef32_pk_fp8_f32 v59, v38, v39, s69 op_sel:[0,0,0,1]
	s_add_i32 s8, s12, 0x4680
	s_cmp_eq_u32 s51, 2
	s_waitcnt lgkmcnt(0)
	v_mfma_f32_32x32x64_f8f6f4 v[18:33], v[178:185], v[52:59], v[18:33]
	ds_read_b128 v[178:181], v177 offset:7680
	ds_read_b128 v[182:185], v177 offset:7696
	s_cselect_b64 s[12:13], -1, 0
	s_and_b64 s[10:11], s[12:13], exec
	s_cselect_b32 s8, 0, s8
	s_add_i32 s8, s8, 0
	s_mov_b64 s[18:19], -1
	v_mfma_f32_32x32x64_f8f6f4 v[66:81], v[66:73], v[98:105], 0
	s_waitcnt lgkmcnt(0)
	v_mfma_f32_32x32x64_f8f6f4 v[2:17], v[178:185], v[52:59], v[2:17]
	v_add_u32_e32 v52, s8, v131
	s_waitcnt vmcnt(7)
	ds_write_b64 v52, v[136:137]
	v_add_u32_e32 v52, s8, v168
	s_and_b32 s8, s23, 0xe00
	s_add_i32 s10, s8, s76
	s_mul_hi_u32 s8, s10, 0xaaaaaaab
	s_lshr_b32 s8, s8, 6
	s_mul_i32 s53, s8, 0xffffffa0
	v_add_u32_e32 v52, 0x1400, v52
	s_add_i32 s53, s53, s10
	s_mov_b64 s[10:11], s[0:1]
	s_waitcnt vmcnt(6)
	ds_write2_b32 v52, v138, v139 offset1:8
	s_waitcnt lgkmcnt(0)
	s_barrier
	s_load_dwordx2 s[16:17], s[10:11], 0xd8
	s_cmp_lt_i32 s53, 64
	s_cselect_b64 s[14:15], -1, 0
	s_cmp_gt_i32 s53, 63
	s_cbranch_scc0 .LBB0_1929
	s_lshl_b64 s[10:11], s[8:9], 20
	s_waitcnt lgkmcnt(0)
	s_add_u32 s10, s16, s10
	s_addc_u32 s11, s17, s11
	s_add_u32 s10, s10, 0x15094000
	s_addc_u32 s11, s11, 0
	s_and_b32 s18, s53, 0x7ffffffc
	s_sub_i32 s52, s18, 64
	s_mov_b64 s[18:19], 0
